# stick-breaking attention: next task-id atomic issued at the start of the task epilogue and waited with vmcnt(63) (no store drain, round trip overlaps the 64 output stores); on top of the K/V load de-s
# speedup vs baseline: 1.0051x; 1.0051x over previous
.LBB0_446:
	s_and_saveexec_b64 s[12:13], s[8:9]
	v_mov_b32_e32 v219, 1
	global_atomic_add v219, v161, v219, s[4:5] sc0
	s_mov_b64 exec, s[12:13]
	s_add_i32 s57, s57, s56
	v_add_u32_e32 v64, s57, v173
	s_lshl_b32 s80, s47, 1
	v_ashrrev_i32_e32 v65, 31, v64
	v_lshl_add_u64 v[66:67], v[144:145], 0, s[80:81]
	v_lshlrev_b64 v[68:69], 12, v[64:65]
	v_cvt_pk_bf16_f32 v48, v48, s0
	v_lshl_add_u64 v[68:69], v[66:67], 0, v[68:69]
	v_or_b32_e32 v70, 2, v64
	global_store_short v[68:69], v48, off
	v_or_b32_e32 v48, 1, v64
	v_ashrrev_i32_e32 v71, 31, v70
	v_cvt_pk_bf16_f32 v65, v49, s0
	v_ashrrev_i32_e32 v49, 31, v48
	v_lshlrev_b64 v[70:71], 12, v[70:71]
	v_lshlrev_b64 v[48:49], 12, v[48:49]
	v_cvt_pk_bf16_f32 v50, v50, s0
	v_lshl_add_u64 v[70:71], v[66:67], 0, v[70:71]
	v_add_u32_e32 v72, 8, v64
	v_lshl_add_u64 v[48:49], v[66:67], 0, v[48:49]
	global_store_short v[70:71], v50, off
	v_or_b32_e32 v50, 3, v64
	v_ashrrev_i32_e32 v73, 31, v72
	global_store_short v[48:49], v65, off
	v_cvt_pk_bf16_f32 v65, v51, s0
	v_ashrrev_i32_e32 v51, 31, v50
	v_lshlrev_b64 v[72:73], 12, v[72:73]
	v_lshlrev_b64 v[50:51], 12, v[50:51]
	v_cvt_pk_bf16_f32 v52, v52, s0
	v_lshl_add_u64 v[72:73], v[66:67], 0, v[72:73]
	v_add_u32_e32 v74, 10, v64
	v_lshl_add_u64 v[50:51], v[66:67], 0, v[50:51]
	global_store_short v[72:73], v52, off
	v_add_u32_e32 v52, 9, v64
	v_ashrrev_i32_e32 v75, 31, v74
	global_store_short v[50:51], v65, off
	v_cvt_pk_bf16_f32 v65, v53, s0
	v_ashrrev_i32_e32 v53, 31, v52
	v_lshlrev_b64 v[74:75], 12, v[74:75]
	v_lshlrev_b64 v[52:53], 12, v[52:53]
	v_cvt_pk_bf16_f32 v54, v54, s0
	v_lshl_add_u64 v[74:75], v[66:67], 0, v[74:75]
	v_add_u32_e32 v76, 16, v64
	v_lshl_add_u64 v[52:53], v[66:67], 0, v[52:53]
	global_store_short v[74:75], v54, off
	v_add_u32_e32 v54, 11, v64
	v_ashrrev_i32_e32 v77, 31, v76
	v_cvt_pk_bf16_f32 v32, v32, s0
	v_cvt_pk_bf16_f32 v16, v16, s0
	v_cvt_pk_bf16_f32 v0, v0, s0
	global_store_short v[52:53], v65, off
	v_cvt_pk_bf16_f32 v65, v55, s0
	v_ashrrev_i32_e32 v55, 31, v54
	v_lshlrev_b64 v[76:77], 12, v[76:77]
	global_store_short v[68:69], v32, off offset:64
	v_cvt_pk_bf16_f32 v32, v33, s0
	global_store_short v[68:69], v16, off offset:128
	v_cvt_pk_bf16_f32 v16, v17, s0
	global_store_short v[68:69], v0, off offset:192
	v_cvt_pk_bf16_f32 v0, v1, s0
	v_lshlrev_b64 v[54:55], 12, v[54:55]
	v_cvt_pk_bf16_f32 v56, v56, s0
	v_lshl_add_u64 v[76:77], v[66:67], 0, v[76:77]
	v_add_u32_e32 v78, 18, v64
	global_store_short v[48:49], v32, off offset:64
	v_cvt_pk_bf16_f32 v32, v34, s0
	global_store_short v[48:49], v16, off offset:128
	v_cvt_pk_bf16_f32 v16, v18, s0
	global_store_short v[48:49], v0, off offset:192
	v_cvt_pk_bf16_f32 v0, v2, s0
	v_lshl_add_u64 v[54:55], v[66:67], 0, v[54:55]
	global_store_short v[76:77], v56, off
	v_add_u32_e32 v56, 17, v64
	v_ashrrev_i32_e32 v79, 31, v78
	global_store_short v[70:71], v32, off offset:64
	v_cvt_pk_bf16_f32 v32, v35, s0
	global_store_short v[70:71], v16, off offset:128
	v_cvt_pk_bf16_f32 v16, v19, s0
	global_store_short v[70:71], v0, off offset:192
	v_cvt_pk_bf16_f32 v0, v3, s0
	global_store_short v[54:55], v65, off
	v_cvt_pk_bf16_f32 v65, v57, s0
	v_ashrrev_i32_e32 v57, 31, v56
	v_lshlrev_b64 v[78:79], 12, v[78:79]
	global_store_short v[50:51], v32, off offset:64
	v_cvt_pk_bf16_f32 v32, v36, s0
	global_store_short v[50:51], v16, off offset:128
	v_cvt_pk_bf16_f32 v16, v20, s0
	global_store_short v[50:51], v0, off offset:192
	v_cvt_pk_bf16_f32 v0, v4, s0
	v_lshlrev_b64 v[56:57], 12, v[56:57]
	v_cvt_pk_bf16_f32 v58, v58, s0
	v_lshl_add_u64 v[78:79], v[66:67], 0, v[78:79]
	s_waitcnt vmcnt(36)
	v_add_u32_e32 v80, 24, v64
	global_store_short v[72:73], v32, off offset:64
	v_cvt_pk_bf16_f32 v32, v37, s0
	global_store_short v[72:73], v16, off offset:128
	v_cvt_pk_bf16_f32 v16, v21, s0
	global_store_short v[72:73], v0, off offset:192
	v_cvt_pk_bf16_f32 v0, v5, s0
	v_lshl_add_u64 v[56:57], v[66:67], 0, v[56:57]
	global_store_short v[78:79], v58, off
	v_add_u32_e32 v58, 19, v64
	v_ashrrev_i32_e32 v81, 31, v80
	global_store_short v[52:53], v32, off offset:64
	v_cvt_pk_bf16_f32 v32, v38, s0
	global_store_short v[52:53], v16, off offset:128
	v_cvt_pk_bf16_f32 v16, v22, s0
	global_store_short v[52:53], v0, off offset:192
	v_cvt_pk_bf16_f32 v0, v6, s0
	global_store_short v[56:57], v65, off
	v_cvt_pk_bf16_f32 v65, v59, s0
	v_ashrrev_i32_e32 v59, 31, v58
	v_lshlrev_b64 v[80:81], 12, v[80:81]
	global_store_short v[74:75], v32, off offset:64
	v_cvt_pk_bf16_f32 v32, v39, s0
	global_store_short v[74:75], v16, off offset:128
	v_cvt_pk_bf16_f32 v16, v23, s0
	global_store_short v[74:75], v0, off offset:192
	v_cvt_pk_bf16_f32 v0, v7, s0
	v_lshlrev_b64 v[58:59], 12, v[58:59]
	v_cvt_pk_bf16_f32 v60, v60, s0
	v_lshl_add_u64 v[80:81], v[66:67], 0, v[80:81]
	v_add_u32_e32 v82, 26, v64
	global_store_short v[54:55], v32, off offset:64
	v_cvt_pk_bf16_f32 v32, v40, s0
	global_store_short v[54:55], v16, off offset:128
	v_cvt_pk_bf16_f32 v16, v24, s0
	global_store_short v[54:55], v0, off offset:192
	v_cvt_pk_bf16_f32 v0, v8, s0
	v_lshl_add_u64 v[58:59], v[66:67], 0, v[58:59]
	global_store_short v[80:81], v60, off
	v_add_u32_e32 v60, 25, v64
	v_ashrrev_i32_e32 v83, 31, v82
	global_store_short v[76:77], v32, off offset:64
	v_cvt_pk_bf16_f32 v32, v41, s0
	global_store_short v[76:77], v16, off offset:128
	v_cvt_pk_bf16_f32 v16, v25, s0
	global_store_short v[76:77], v0, off offset:192
	v_cvt_pk_bf16_f32 v0, v9, s0
	global_store_short v[58:59], v65, off
	v_cvt_pk_bf16_f32 v65, v61, s0
	v_ashrrev_i32_e32 v61, 31, v60
	v_lshlrev_b64 v[82:83], 12, v[82:83]
	global_store_short v[56:57], v32, off offset:64
	v_cvt_pk_bf16_f32 v32, v42, s0
	global_store_short v[56:57], v16, off offset:128
	v_cvt_pk_bf16_f32 v16, v26, s0
	global_store_short v[56:57], v0, off offset:192
	v_cvt_pk_bf16_f32 v0, v10, s0
	v_lshlrev_b64 v[60:61], 12, v[60:61]
	v_cvt_pk_bf16_f32 v62, v62, s0
	v_lshl_add_u64 v[82:83], v[66:67], 0, v[82:83]
	global_store_short v[78:79], v32, off offset:64
	v_cvt_pk_bf16_f32 v32, v43, s0
	global_store_short v[78:79], v16, off offset:128
	v_cvt_pk_bf16_f32 v16, v27, s0
	global_store_short v[78:79], v0, off offset:192
	v_cvt_pk_bf16_f32 v0, v11, s0
	v_lshl_add_u64 v[60:61], v[66:67], 0, v[60:61]
	global_store_short v[82:83], v62, off
	v_add_u32_e32 v62, 27, v64
	global_store_short v[58:59], v32, off offset:64
	v_cvt_pk_bf16_f32 v32, v44, s0
	global_store_short v[58:59], v16, off offset:128
	v_cvt_pk_bf16_f32 v16, v28, s0
	global_store_short v[58:59], v0, off offset:192
	v_cvt_pk_bf16_f32 v0, v12, s0
	global_store_short v[60:61], v65, off
	v_cvt_pk_bf16_f32 v65, v63, s0
	v_ashrrev_i32_e32 v63, 31, v62
	global_store_short v[80:81], v32, off offset:64
	v_cvt_pk_bf16_f32 v32, v45, s0
	global_store_short v[80:81], v16, off offset:128
	v_cvt_pk_bf16_f32 v16, v29, s0
	global_store_short v[80:81], v0, off offset:192
	v_cvt_pk_bf16_f32 v0, v13, s0
	v_lshlrev_b64 v[62:63], 12, v[62:63]
	global_store_short v[60:61], v32, off offset:64
	v_cvt_pk_bf16_f32 v32, v46, s0
	global_store_short v[60:61], v16, off offset:128
	v_cvt_pk_bf16_f32 v16, v30, s0
	global_store_short v[60:61], v0, off offset:192
	v_cvt_pk_bf16_f32 v0, v14, s0
	v_lshl_add_u64 v[62:63], v[66:67], 0, v[62:63]
	global_store_short v[82:83], v32, off offset:64
	v_cvt_pk_bf16_f32 v32, v47, s0
	global_store_short v[82:83], v16, off offset:128
	v_cvt_pk_bf16_f32 v16, v31, s0
	global_store_short v[82:83], v0, off offset:192
	v_cvt_pk_bf16_f32 v0, v15, s0
	global_store_short v[62:63], v65, off
	global_store_short v[62:63], v32, off offset:64
	global_store_short v[62:63], v16, off offset:128
	global_store_short v[62:63], v0, off offset:192

.LBB0_448:
	s_waitcnt vmcnt(63)
	v_readfirstlane_b32 s10, v219
	s_cmpk_gt_i32 s10, 0x7ff
	s_cselect_b64 s[30:31], -1, 0
	s_and_b64 vcc, exec, s[30:31]
	s_cbranch_vccnz .LBB0_447
	s_lshl_b32 s14, s10, 1
	s_and_b32 s47, s10, 0x780
	s_lshl_b32 s11, s10, 5
	s_add_i32 s10, s14, s46
	s_and_b32 s56, s11, 0xfe0
	s_and_b32 s57, s10, 0xfffff000
	s_or_b32 s15, s57, s56
	s_lshl_b32 s10, s47, 1
	s_add_u32 s10, s50, s10
	s_addc_u32 s11, s51, 0
	v_add_u32_e32 v32, s15, v174
	v_mov_b64_e32 v[24:25], s[10:11]
	v_add_u32_e32 v34, s15, v175
	v_add_u32_e32 v36, s15, v176
	v_add_u32_e32 v38, s15, v177
	v_add_u32_e32 v40, s15, v178
	v_add_u32_e32 v41, s15, v179
	v_mad_i64_i32 v[0:1], s[12:13], v32, s3, v[24:25]
	v_mad_i64_i32 v[2:3], s[12:13], v34, s3, v[24:25]
	v_mad_i64_i32 v[8:9], s[12:13], v36, s3, v[24:25]
	v_mad_i64_i32 v[10:11], s[12:13], v38, s3, v[24:25]
	v_mad_i64_i32 v[16:17], s[12:13], v40, s3, v[24:25]
	v_mad_i64_i32 v[18:19], s[12:13], v41, s3, v[24:25]
	v_lshl_add_u64 v[0:1], v[0:1], 0, v[160:161]
	v_lshl_add_u64 v[4:5], v[2:3], 0, v[160:161]
	v_lshl_add_u64 v[8:9], v[8:9], 0, v[160:161]
	v_lshl_add_u64 v[12:13], v[10:11], 0, v[160:161]
	v_lshl_add_u64 v[16:17], v[16:17], 0, v[160:161]
	v_lshl_add_u64 v[20:21], v[18:19], 0, v[160:161]
	global_load_dwordx4 v[0:3], v[0:1], off
	s_nop 0
	global_load_dwordx4 v[4:7], v[4:5], off
	s_nop 0
	global_load_dwordx4 v[8:11], v[8:9], off
	s_nop 0
	global_load_dwordx4 v[12:15], v[12:13], off
	s_nop 0
	global_load_dwordx4 v[16:19], v[16:17], off
	s_nop 0
	global_load_dwordx4 v[20:23], v[20:21], off
	v_mov_b32_e32 v147, v161
	v_lshl_add_u64 v[148:149], s[10:11], 0, v[146:147]
	s_mov_b64 s[98:99], 0x2000
	v_lshl_add_u64 v[216:217], v[148:149], 0, s[98:99]
	v_mad_i64_i32 v[32:33], s[10:11], v32, s3, v[148:149]
	v_add_co_u32_e32 v32, vcc, s93, v32
	v_mad_i64_i32 v[34:35], s[10:11], v34, s3, v[148:149]
	s_nop 0
	v_addc_co_u32_e32 v33, vcc, 0, v33, vcc
	v_add_co_u32_e32 v34, vcc, s93, v34
	v_mad_i64_i32 v[36:37], s[10:11], v36, s3, v[148:149]
	s_nop 0
	v_addc_co_u32_e32 v35, vcc, 0, v35, vcc
	v_add_u32_e32 v42, s15, v180
	v_add_u32_e32 v43, s15, v181
	v_add_co_u32_e32 v36, vcc, s93, v36
	v_mad_i64_i32 v[26:27], s[12:13], v42, s3, v[24:25]
	v_mad_i64_i32 v[24:25], s[12:13], v43, s3, v[24:25]
	v_mad_i64_i32 v[38:39], s[10:11], v38, s3, v[148:149]
	v_addc_co_u32_e32 v37, vcc, 0, v37, vcc
	v_lshl_add_u64 v[26:27], v[26:27], 0, v[160:161]
	v_lshl_add_u64 v[28:29], v[24:25], 0, v[160:161]
	v_add_co_u32_e32 v38, vcc, s93, v38
	global_load_dwordx4 v[24:27], v[26:27], off
	s_nop 0
	global_load_dwordx4 v[28:31], v[28:29], off
	v_addc_co_u32_e32 v39, vcc, 0, v39, vcc
	global_load_dwordx4 v[80:83], v[32:33], off offset:-4096
	global_load_dwordx4 v[84:87], v[32:33], off
	global_load_dwordx4 v[88:91], v[34:35], off offset:-4096
	global_load_dwordx4 v[92:95], v[34:35], off
	global_load_dwordx4 v[96:99], v[36:37], off offset:-4096
	global_load_dwordx4 v[100:103], v[36:37], off
	global_load_dwordx4 v[104:107], v[38:39], off offset:-4096
	global_load_dwordx4 v[108:111], v[38:39], off
	v_mad_i64_i32 v[32:33], s[10:11], v40, s3, v[216:217]
	v_mad_i64_i32 v[34:35], s[10:11], v41, s3, v[216:217]
	v_mad_i64_i32 v[44:45], s[10:11], v42, s3, v[216:217]
	v_mad_i64_i32 v[46:47], s[10:11], v43, s3, v[216:217]
	global_load_dwordx4 v[112:115], v[32:33], off offset:-4096
	global_load_dwordx4 v[116:119], v[32:33], off
	global_load_dwordx4 v[120:123], v[34:35], off offset:-4096
	global_load_dwordx4 v[124:127], v[34:35], off
	global_load_dwordx4 v[128:131], v[44:45], off offset:-4096
	global_load_dwordx4 v[132:135], v[44:45], off
	global_load_dwordx4 v[136:139], v[46:47], off offset:-4096
	global_load_dwordx4 v[140:143], v[46:47], off
	v_mov_b32_e32 v48, 0
	s_mov_b32 s58, 0
	v_mov_b32_e32 v205, 1.0
	v_mov_b32_e32 v49, v48
	v_mov_b32_e32 v50, v48
	v_mov_b32_e32 v51, v48
	v_mov_b32_e32 v52, v48
	v_mov_b32_e32 v53, v48
	v_mov_b32_e32 v54, v48
	v_mov_b32_e32 v55, v48
	v_mov_b32_e32 v56, v48
	v_mov_b32_e32 v57, v48
	v_mov_b32_e32 v58, v48
	v_mov_b32_e32 v59, v48
	v_mov_b32_e32 v60, v48
	v_mov_b32_e32 v61, v48
	v_mov_b32_e32 v62, v48
	s_add_i32 s10, s43, s14
	s_and_b32 s10, s10, 0xfffff000
	s_or_b32 s10, s56, s10
	s_waitcnt vmcnt(16)
	ds_write_b128 v190, v[0:3] offset:8192
	ds_write_b128 v191, v[4:7] offset:8192
	ds_write_b128 v192, v[8:11] offset:8192
	ds_write_b128 v193, v[12:15] offset:8192
	ds_write_b128 v194, v[16:19] offset:8192
	ds_write_b128 v195, v[20:23] offset:8192
	ds_write_b128 v196, v[24:27] offset:8192
	ds_write_b128 v197, v[28:31] offset:8192
	v_add_u32_e32 v147, s10, v182
	v_add_u32_e32 v198, s10, v183
	v_add_u32_e32 v199, s10, v184
	v_add_u32_e32 v200, s10, v185
	v_add_u32_e32 v201, s10, v186
	v_add_u32_e32 v202, s10, v187
	v_add_u32_e32 v203, s10, v188
	v_add_u32_e32 v204, s10, v189
	v_mov_b32_e32 v63, v48
	v_mov_b32_e32 v32, v48
	v_mov_b32_e32 v33, v48
	v_mov_b32_e32 v34, v48
	v_mov_b32_e32 v35, v48
	v_mov_b32_e32 v36, v48
	v_mov_b32_e32 v37, v48
	v_mov_b32_e32 v38, v48
	v_mov_b32_e32 v39, v48
	v_mov_b32_e32 v40, v48
	v_mov_b32_e32 v41, v48
	v_mov_b32_e32 v42, v48
	v_mov_b32_e32 v43, v48
	v_mov_b32_e32 v44, v48
	v_mov_b32_e32 v45, v48
	v_mov_b32_e32 v46, v48
	v_mov_b32_e32 v47, v48
	v_mov_b32_e32 v16, v48
	v_mov_b32_e32 v17, v48
	v_mov_b32_e32 v18, v48
	v_mov_b32_e32 v19, v48
	v_mov_b32_e32 v20, v48
	v_mov_b32_e32 v21, v48
	v_mov_b32_e32 v22, v48
	v_mov_b32_e32 v23, v48
	v_mov_b32_e32 v24, v48
	v_mov_b32_e32 v25, v48
	v_mov_b32_e32 v26, v48
	v_mov_b32_e32 v27, v48
	v_mov_b32_e32 v28, v48
	v_mov_b32_e32 v29, v48
	v_mov_b32_e32 v30, v48
	v_mov_b32_e32 v31, v48
	v_mov_b32_e32 v0, v48
	v_mov_b32_e32 v1, v48
	v_mov_b32_e32 v2, v48
	v_mov_b32_e32 v3, v48
	v_mov_b32_e32 v4, v48
	v_mov_b32_e32 v5, v48
	v_mov_b32_e32 v6, v48
	v_mov_b32_e32 v7, v48
	v_mov_b32_e32 v8, v48
	v_mov_b32_e32 v9, v48
	v_mov_b32_e32 v10, v48
	v_mov_b32_e32 v11, v48
	v_mov_b32_e32 v12, v48
	v_mov_b32_e32 v13, v48
	v_mov_b32_e32 v14, v48
	v_mov_b32_e32 v15, v48
	s_branch .LBB0_455
